# cache policy: sc1 (L1 bypass) on GEMM1 weight-tile loads, sc1 on agg output stores; plus agg barrier to epilogue, pool 16 loads in flight, gemm1 static setprio for waves 4-7
# baseline (speedup 1.0000x reference)
.Lagg_nobar:
	s_load_dwordx4 s[4:7], s[0:1], 0x40
	s_and_saveexec_b64 s[0:1], s[2:3]
	s_cbranch_execz .LBB3_119
	s_mov_b64 s[0:1], -1
	s_andn2_b64 vcc, exec, s[14:15]
	v_ashrrev_i32_e32 v49, 31, v48
	s_cbranch_vccnz .LBB3_117
	v_lshl_add_u64 v[4:5], s[12:13], 0, v[48:49]
	v_lshlrev_b64 v[4:5], 7, v[4:5]
	s_waitcnt lgkmcnt(0)
	v_lshl_add_u64 v[4:5], s[6:7], 0, v[4:5]
	v_mov_b32_e32 v51, 0
	v_cvt_pk_f16_f32 v3, v52, v53
	v_cvt_pk_f16_f32 v2, v54, v55
	v_cvt_pk_f16_f32 v1, v56, v57
	v_cvt_pk_f16_f32 v0, v58, v59
	v_lshl_add_u64 v[4:5], v[4:5], 0, v[50:51]
	s_mov_b64 s[0:1], 0
	global_store_dwordx4 v[4:5], v[0:3], off sc1
.LBB3_117:
	s_andn2_b64 vcc, exec, s[0:1]
	s_cbranch_vccnz .LBB3_119
	v_lshlrev_b32_e32 v12, 5, v60
	ds_read_b128 v[4:7], v12 offset:8704
	ds_read_b128 v[8:11], v12 offset:8448
	ds_read_b128 v[0:3], v12 offset:8464
	ds_read_b128 v[12:15], v12 offset:8720
	s_mov_b32 s1, 0
	s_lshl_b32 s0, s28, 7
	s_waitcnt lgkmcnt(0)
	v_pk_fma_f32 v[4:5], v[58:59], v[8:9], v[4:5]
	v_pk_fma_f32 v[6:7], v[56:57], v[10:11], v[6:7]
	v_mul_f32_e32 v8, 0x3fb8aa3b, v4
	v_mul_f32_e32 v9, 0x3fb8aa3b, v5
	v_exp_f32_e32 v8, v8
	v_exp_f32_e32 v9, v9
	v_cmp_lt_f32_e32 vcc, 0, v5
	v_pk_fma_f32 v[0:1], v[54:55], v[0:1], v[12:13]
	v_pk_fma_f32 v[2:3], v[52:53], v[2:3], v[14:15]
	v_pk_add_f32 v[8:9], v[8:9], -1.0 op_sel_hi:[1,0]
	v_mov_b32_e32 v51, 0
	v_cndmask_b32_e32 v5, v9, v5, vcc
	v_mul_f32_e32 v9, 0x3fb8aa3b, v6
	v_exp_f32_e32 v10, v9
	v_mul_f32_e32 v9, 0x3fb8aa3b, v7
	v_exp_f32_e32 v11, v9
	v_cmp_lt_f32_e32 vcc, 0, v4
	s_nop 1
	v_cndmask_b32_e32 v4, v8, v4, vcc
	v_pk_add_f32 v[8:9], v[10:11], -1.0 op_sel_hi:[1,0]
	v_cmp_lt_f32_e32 vcc, 0, v7
	v_cvt_pk_f16_f32 v4, v4, v5
	s_nop 0
	v_cndmask_b32_e32 v5, v9, v7, vcc
	v_mul_f32_e32 v7, 0x3fb8aa3b, v0
	v_exp_f32_e32 v10, v7
	v_mul_f32_e32 v7, 0x3fb8aa3b, v1
	v_exp_f32_e32 v11, v7
	v_cmp_lt_f32_e32 vcc, 0, v6
	s_nop 1
	v_cndmask_b32_e32 v6, v8, v6, vcc
	v_cvt_pk_f16_f32 v5, v6, v5
	v_pk_add_f32 v[6:7], v[10:11], -1.0 op_sel_hi:[1,0]
	v_cmp_lt_f32_e32 vcc, 0, v1
	s_nop 1
	v_cndmask_b32_e32 v1, v7, v1, vcc
	v_mul_f32_e32 v7, 0x3fb8aa3b, v2
	v_exp_f32_e32 v8, v7
	v_mul_f32_e32 v7, 0x3fb8aa3b, v3
	v_exp_f32_e32 v9, v7
	v_cmp_lt_f32_e32 vcc, 0, v0
	s_nop 1
	v_cndmask_b32_e32 v0, v6, v0, vcc
	v_cvt_pk_f16_f32 v6, v0, v1
	v_pk_add_f32 v[0:1], v[8:9], -1.0 op_sel_hi:[1,0]
	v_cmp_lt_f32_e32 vcc, 0, v3
	s_nop 1
	v_cndmask_b32_e32 v1, v1, v3, vcc
	v_cmp_lt_f32_e32 vcc, 0, v2
	s_nop 1
	v_cndmask_b32_e32 v0, v0, v2, vcc
	v_cvt_pk_f16_f32 v7, v0, v1
	v_lshlrev_b64 v[0:1], 9, v[48:49]
	v_lshl_add_u64 v[0:1], s[4:5], 0, v[0:1]
	v_lshl_add_u64 v[0:1], v[0:1], 0, s[0:1]
	v_lshl_add_u64 v[0:1], v[0:1], 0, v[50:51]
	global_store_dwordx4 v[0:1], v[4:7], off sc1

.LBB6_104:
	s_load_dwordx4 s[12:15], s[0:1], 0x8
	v_lshrrev_b32_e32 v1, 4, v0
	v_add_u32_e32 v2, s16, v1
	v_sub_u32_e32 v2, 0, v2
	v_and_b32_e32 v199, 3, v2
	v_lshlrev_b32_e32 v2, 2, v0
	s_waitcnt lgkmcnt(0)
	s_min_i32 s2, s14, 0
	v_and_b32_e32 v10, 60, v2
	v_lshl_or_b32 v2, s2, 6, v10
	v_mad_i32_i24 v2, v199, -8, v2
	s_sub_i32 s15, s8, s16
	v_max_i32_e32 v2, 0, v2
	s_add_i32 s8, s13, -4
	v_min_i32_e32 v2, s8, v2
	v_ashrrev_i32_e32 v3, 31, v2
	s_add_i32 s9, s15, -1
	v_lshl_add_u64 v[12:13], v[2:3], 2, s[4:5]
	v_min_i32_e32 v2, s9, v1
	v_add_u32_e32 v2, s16, v2
	v_mad_i64_i32 v[2:3], s[2:3], v2, s12, 0
	v_lshlrev_b64 v[186:187], 2, v[2:3]
	v_or_b32_e32 v2, 32, v1
	v_min_i32_e32 v2, s9, v2
	v_add_u32_e32 v2, s16, v2
	v_or_b32_e32 v11, 64, v1
	v_mad_i64_i32 v[2:3], s[2:3], v2, s12, 0
	v_min_i32_e32 v11, s9, v11
	v_or_b32_e32 v1, 0x60, v1
	v_lshl_add_u64 v[14:15], v[12:13], 0, v[186:187]
	v_lshlrev_b64 v[188:189], 2, v[2:3]
	v_add_u32_e32 v11, s16, v11
	v_min_i32_e32 v1, s9, v1
	v_lshl_add_u64 v[16:17], v[12:13], 0, v[188:189]
	global_load_dwordx4 v[6:9], v[14:15], off nt
	global_load_dwordx4 v[2:5], v[16:17], off nt
	v_mad_i64_i32 v[14:15], s[2:3], v11, s12, 0
	v_add_u32_e32 v1, s16, v1
	v_lshlrev_b64 v[190:191], 2, v[14:15]
	v_mad_i64_i32 v[14:15], s[2:3], v1, s12, 0
	s_add_i32 s9, s14, -1
	s_min_i32 s2, s9, 0
	s_ashr_i32 s3, s2, 31
	s_lshl_b64 s[2:3], s[2:3], 15
	s_add_u32 s12, s6, s2
	s_addc_u32 s13, s7, s3
	v_lshlrev_b32_e32 v184, 4, v0
	v_mov_b32_e32 v185, 0
	v_lshl_add_u64 v[24:25], s[12:13], 0, v[184:185]
	s_movk_i32 s10, 0x2000
	s_min_i32 s2, s14, 1
	v_add_co_u32_e32 v32, vcc, s10, v24
	v_lshl_or_b32 v1, s2, 6, v10
	v_lshlrev_b64 v[192:193], 2, v[14:15]
	v_addc_co_u32_e32 v33, vcc, 0, v25, vcc
	s_movk_i32 s11, 0x6000
	v_mad_i32_i24 v1, v199, -8, v1
	v_lshl_add_u64 v[20:21], v[12:13], 0, v[190:191]
	v_lshl_add_u64 v[22:23], v[12:13], 0, v[192:193]
	v_add_co_u32_e32 v34, vcc, s11, v24
	v_max_i32_e32 v1, 0, v1
	s_min_i32 s2, s9, 1
	global_load_dwordx4 v[12:15], v[20:21], off nt
	global_load_dwordx4 v[16:19], v[22:23], off nt
	v_addc_co_u32_e32 v35, vcc, 0, v25, vcc
	global_load_dwordx4 v[20:23], v184, s[12:13] sc1
	global_load_dwordx4 v[24:27], v[32:33], off sc1
	global_load_dwordx4 v[28:31], v[34:35], off sc1
	v_min_i32_e32 v32, s8, v1
	s_ashr_i32 s3, s2, 31
	v_ashrrev_i32_e32 v33, 31, v32
	s_lshl_b64 s[2:3], s[2:3], 15
	v_lshl_add_u64 v[40:41], v[32:33], 2, s[4:5]
	s_add_u32 s2, s6, s2
	v_or_b32_e32 v182, 0x4000, v184
	v_lshl_add_u64 v[42:43], v[40:41], 0, v[186:187]
	v_lshl_add_u64 v[44:45], v[40:41], 0, v[188:189]
	v_lshl_add_u64 v[48:49], v[40:41], 0, v[190:191]
	v_lshl_add_u64 v[50:51], v[40:41], 0, v[192:193]
	s_addc_u32 s3, s7, s3
	global_load_dwordx4 v[32:35], v[42:43], off nt
	global_load_dwordx4 v[36:39], v[44:45], off nt
	s_nop 0
	global_load_dwordx4 v[40:43], v[48:49], off nt
	global_load_dwordx4 v[44:47], v[50:51], off nt
	v_lshl_add_u64 v[52:53], s[2:3], 0, v[184:185]
	global_load_dwordx4 v[48:51], v182, s[12:13] sc1
	global_load_dwordx4 v[110:113], v182, s[2:3] sc1
	s_min_i32 s12, s14, 2
	v_add_co_u32_e32 v54, vcc, s10, v52
	v_lshl_or_b32 v1, s12, 6, v10
	s_nop 0
	v_addc_co_u32_e32 v55, vcc, 0, v53, vcc
	v_mad_i32_i24 v1, v199, -8, v1
	v_add_co_u32_e32 v52, vcc, s11, v52
	v_max_i32_e32 v1, 0, v1
	s_nop 0
	v_addc_co_u32_e32 v53, vcc, 0, v53, vcc
	global_load_dwordx4 v[122:125], v[54:55], off sc1
	global_load_dwordx4 v[118:121], v[52:53], off sc1
	v_min_i32_e32 v52, s8, v1
	v_ashrrev_i32_e32 v53, 31, v52
	s_min_i32 s12, s14, 3
	v_lshl_add_u64 v[52:53], v[52:53], 2, s[4:5]
	v_lshl_or_b32 v1, s12, 6, v10
	v_lshl_add_u64 v[54:55], v[52:53], 0, v[186:187]
	v_mad_i32_i24 v1, v199, -8, v1
	v_lshl_add_u64 v[56:57], v[52:53], 0, v[188:189]
	global_load_dwordx4 v[94:97], v[54:55], off nt
	global_load_dwordx4 v[90:93], v[56:57], off nt
	v_lshl_add_u64 v[54:55], v[52:53], 0, v[190:191]
	v_lshl_add_u64 v[52:53], v[52:53], 0, v[192:193]
	v_max_i32_e32 v1, 0, v1
	global_load_dwordx4 v[86:89], v[54:55], off nt
	global_load_dwordx4 v[82:85], v[52:53], off nt
	v_min_i32_e32 v52, s8, v1
	s_min_i32 s12, s9, 2
	v_ashrrev_i32_e32 v53, 31, v52
	s_ashr_i32 s13, s12, 31
	v_lshl_add_u64 v[52:53], v[52:53], 2, s[4:5]
	s_lshl_b64 s[12:13], s[12:13], 15
	v_lshl_add_u64 v[54:55], v[52:53], 0, v[186:187]
	s_add_u32 s12, s6, s12
	v_lshl_add_u64 v[56:57], v[52:53], 0, v[188:189]
	global_load_dwordx4 v[78:81], v[54:55], off nt
	global_load_dwordx4 v[74:77], v[56:57], off nt
	v_lshl_add_u64 v[54:55], v[52:53], 0, v[190:191]
	v_lshl_add_u64 v[52:53], v[52:53], 0, v[192:193]
	s_addc_u32 s13, s7, s13
	global_load_dwordx4 v[70:73], v[54:55], off nt
	global_load_dwordx4 v[66:69], v[52:53], off nt
	v_lshl_add_u64 v[52:53], s[12:13], 0, v[184:185]
	v_add_co_u32_e32 v54, vcc, s10, v52
	global_load_dwordx4 v[126:129], v184, s[2:3] sc1
	global_load_dwordx4 v[106:109], v184, s[12:13] sc1
	v_addc_co_u32_e32 v55, vcc, 0, v53, vcc
	v_add_co_u32_e32 v52, vcc, s11, v52
	global_load_dwordx4 v[98:101], v182, s[12:13] sc1
	s_nop 0
	v_addc_co_u32_e32 v53, vcc, 0, v53, vcc
	global_load_dwordx4 v[114:117], v[54:55], off sc1
	global_load_dwordx4 v[102:105], v[52:53], off sc1
	v_bfe_u32 v203, v0, 1, 3
	v_sub_u32_e32 v205, v203, v199
	v_add_u32_e32 v1, 24, v205
	v_cmp_gt_i32_e32 vcc, 0, v205
	s_movk_i32 s3, 0x178
	v_mov_b32_e32 v206, 0xc180
	v_cndmask_b32_e32 v1, v205, v1, vcc
	v_mul_i32_i24_e32 v1, 0x810, v1
	v_cmp_gt_u32_e32 vcc, s3, v205
	v_lshlrev_b32_e32 v195, 3, v0
	v_and_b32_e32 v204, 8, v195
	v_cndmask_b32_e32 v1, v206, v1, vcc
	v_or_b32_e32 v1, v1, v204
	v_and_b32_e32 v202, 0x1f0, v0
	v_add_u32_e32 v1, v1, v202
	s_waitcnt vmcnt(27)
	v_cvt_pk_f16_f32 v9, v8, v9
	v_cvt_pk_f16_f32 v8, v6, v7
	s_waitcnt vmcnt(26)
	v_cvt_pk_f16_f32 v5, v4, v5
	v_cvt_pk_f16_f32 v4, v2, v3
	ds_write2st64_b64 v1, v[8:9], v[4:5] offset1:1
	s_waitcnt vmcnt(25)
	v_cvt_pk_f16_f32 v3, v14, v15
	v_cvt_pk_f16_f32 v2, v12, v13
	s_waitcnt vmcnt(24)
	v_cvt_pk_f16_f32 v5, v18, v19
	v_cvt_pk_f16_f32 v4, v16, v17
	ds_write2st64_b64 v1, v[2:3], v[4:5] offset0:2 offset1:3
	v_add_u32_e32 v1, 0x10990, v184
	s_waitcnt vmcnt(23)
	ds_write_b128 v184, v[20:23] offset:51600
	s_waitcnt vmcnt(22)
	ds_write_b128 v184, v[24:27] offset:59792
	s_waitcnt vmcnt(16)
	ds_write_b128 v1, v[48:51]
	v_add_u32_e32 v1, 0x12990, v184
	ds_write_b128 v1, v[28:31]
	v_mul_i32_i24_e32 v1, 0x810, v205
	v_or_b32_e32 v1, v1, v204
	v_add_u32_e32 v1, v1, v202
	v_cvt_pk_f16_f32 v3, v34, v35
	v_cvt_pk_f16_f32 v2, v32, v33
	v_cvt_pk_f16_f32 v5, v38, v39
	v_cvt_pk_f16_f32 v4, v36, v37
	v_add_u32_e32 v1, 0x80, v1
	v_and_b32_e32 v194, 31, v0
	ds_write2st64_b64 v1, v[2:3], v[4:5] offset0:32 offset1:33
	v_cvt_pk_f16_f32 v3, v42, v43
	v_cvt_pk_f16_f32 v2, v40, v41
	v_cvt_pk_f16_f32 v5, v46, v47
	v_cvt_pk_f16_f32 v4, v44, v45
	v_bfe_u32 v197, v0, 5, 1
	v_bfe_u32 v196, v0, 6, 2
	s_mov_b32 s18, 0
	v_or_b32_e32 v200, 0x6000, v184
	s_movk_i32 s2, 0x810
	v_lshrrev_b32_e32 v198, 8, v0
	ds_write2st64_b64 v1, v[2:3], v[4:5] offset0:34 offset1:35
	s_cmp_lt_i32 s14, 4
	s_mov_b32 s12, 0
	v_lshlrev_b32_e32 v1, 4, v194
	v_lshlrev_b32_e32 v201, 12, v197
	s_waitcnt lgkmcnt(0)
	s_barrier
	s_cbranch_scc1 .LBB6_108
	v_readfirstlane_b32 s40, v198
	s_cmp_eq_u32 s40, 0
	s_cbranch_scc1 .Lg1_noprio
	s_setprio 1

.LBB6_106:
	s_mov_b32 s18, s12
	s_add_i32 s21, s13, 1
	s_add_i32 s12, s12, 4
	v_add_u32_e32 v225, v201, v209
	s_cmp_lg_u32 s13, 2
	ds_read_b128 v[162:165], v225 offset:51600
	s_cselect_b32 s21, s21, 0
	s_mul_i32 s19, s13, 0x4080
	s_add_i32 s13, s21, 1
	s_cmp_lg_u32 s21, 2
	v_add3_u32 v174, s19, v207, v208
	s_cselect_b32 s13, s13, 0
	ds_read_b128 v[166:169], v225 offset:52112
	ds_read_b128 v[170:173], v174
	ds_read_b128 v[174:177], v174 offset:512
	s_lshl_b32 s22, s13, 3
	s_waitcnt vmcnt(19)
	v_cvt_pk_f16_f32 v93, v92, v93
	v_cvt_pk_f16_f32 v92, v90, v91
	v_sub_u32_e32 v90, s22, v199
	v_add_u32_e32 v90, v90, v203
	v_add_u32_e32 v91, 24, v90
	v_cmp_gt_i32_e32 vcc, 0, v90
	v_subrev_u32_e32 v178, 24, v215
	s_waitcnt lgkmcnt(1)
	v_mfma_f32_32x32x16_f16 v[2:17], v[162:165], v[170:173], v[2:17]
	v_cndmask_b32_e32 v90, v90, v91, vcc
	v_mul_lo_u32 v90, v90, s2
	v_cmp_gt_u32_e32 vcc, s3, v178
	v_cvt_pk_f16_f32 v97, v96, v97
	v_cvt_pk_f16_f32 v96, v94, v95
	v_cndmask_b32_e32 v90, v206, v90, vcc
	s_waitcnt vmcnt(18)
	v_cvt_pk_f16_f32 v89, v88, v89
	s_waitcnt lgkmcnt(0)
	v_mfma_f32_32x32x16_f16 v[50:65], v[162:165], v[174:177], v[50:65]
	v_add3_u32 v162, s19, v210, v208
	v_cvt_pk_f16_f32 v88, v86, v87
	s_waitcnt vmcnt(17)
	v_cvt_pk_f16_f32 v85, v84, v85
	v_cvt_pk_f16_f32 v84, v82, v83
	s_mul_i32 s24, s21, 0x4080
	s_add_i32 s21, s18, 3
	s_min_i32 s22, s21, s9
	v_mfma_f32_32x32x16_f16 v[34:49], v[166:169], v[170:173], v[34:49]
	v_add_u32_e32 v170, v214, v90
	ds_write2st64_b64 v170, v[96:97], v[92:93] offset1:1
	v_add3_u32 v172, s19, v212, v208
	v_add_u32_e32 v223, 0x14990, v184
	v_add_u32_e32 v224, 0x14990, v182
	v_add3_u32 v230, s24, v207, v208
	s_waitcnt vmcnt(15)
	v_cvt_pk_f16_f32 v77, v76, v77
	v_mfma_f32_32x32x16_f16 v[18:33], v[166:169], v[174:177], v[18:33]
	ds_read_b128 v[90:93], v216 offset:51600
	ds_read_b128 v[94:97], v162
	ds_read_b128 v[162:165], v162 offset:512
	ds_read_b128 v[166:169], v216 offset:52112
	ds_write2st64_b64 v170, v[88:89], v[84:85] offset0:2 offset1:3
	v_cvt_pk_f16_f32 v76, v74, v75
	v_cvt_pk_f16_f32 v81, v80, v81
	v_cvt_pk_f16_f32 v80, v78, v79
	s_waitcnt vmcnt(14)
	v_cvt_pk_f16_f32 v73, v72, v73
	v_cvt_pk_f16_f32 v72, v70, v71
	s_waitcnt lgkmcnt(3)
	v_mfma_f32_32x32x16_f16 v[2:17], v[90:93], v[94:97], v[2:17]
	s_waitcnt vmcnt(13)
	v_cvt_pk_f16_f32 v69, v68, v69
	v_cvt_pk_f16_f32 v68, v66, v67
	s_waitcnt lgkmcnt(2)
	v_mfma_f32_32x32x16_f16 v[50:65], v[90:93], v[162:165], v[50:65]
	v_add3_u32 v90, s19, v211, v208
	s_add_i32 s19, s18, 6
	s_min_i32 s23, s19, s14
	s_waitcnt lgkmcnt(1)
	v_mfma_f32_32x32x16_f16 v[34:49], v[166:169], v[94:97], v[34:49]
	ds_read_b128 v[82:85], v217 offset:51600
	ds_read_b128 v[86:89], v90
	ds_read_b128 v[90:93], v90 offset:512
	ds_read_b128 v[94:97], v217 offset:52112
	s_waitcnt vmcnt(9)
	ds_write_b128 v223, v[126:129]
	ds_write_b128 v223, v[122:125] offset:8192
	v_mfma_f32_32x32x16_f16 v[18:33], v[166:169], v[162:165], v[18:33]
	v_lshl_add_u32 v162, s23, 6, v213
	s_ashr_i32 s23, s22, 31
	s_lshl_b64 s[22:23], s[22:23], 15
	s_add_u32 s22, s6, s22
	s_addc_u32 s23, s7, s23
	s_add_i32 s21, s13, 1
	s_cmp_lg_u32 s13, 2
	s_waitcnt lgkmcnt(4)
	v_mfma_f32_32x32x16_f16 v[2:17], v[82:85], v[86:89], v[2:17]
	s_cselect_b32 s21, s21, 0
	s_waitcnt lgkmcnt(3)
	v_mfma_f32_32x32x16_f16 v[50:65], v[82:85], v[90:93], v[50:65]
	v_max_i32_e32 v82, 0, v162
	v_min_i32_e32 v82, s8, v82
	v_ashrrev_i32_e32 v83, 31, v82
	v_lshl_add_u64 v[170:171], v[82:83], 2, s[4:5]
	ds_read_b128 v[82:85], v218 offset:51600
	ds_read_b128 v[162:165], v218 offset:52112
	ds_read_b128 v[126:129], v172
	ds_read_b128 v[166:169], v172 offset:512
	v_lshl_add_u64 v[174:175], v[170:171], 0, v[186:187]
	s_waitcnt lgkmcnt(6)
	v_mfma_f32_32x32x16_f16 v[34:49], v[94:97], v[86:89], v[34:49]
	v_lshl_add_u64 v[86:87], s[22:23], 0, v[184:185]
	v_add_co_u32_e32 v226, vcc, s10, v86
	v_lshl_add_u64 v[88:89], s[22:23], 0, v[182:183]
	s_nop 0
	v_addc_co_u32_e32 v227, vcc, 0, v87, vcc
	v_lshl_add_u64 v[176:177], v[170:171], 0, v[188:189]
	v_mfma_f32_32x32x16_f16 v[18:33], v[94:97], v[90:93], v[18:33]
	global_load_dwordx4 v[122:125], v[86:87], off sc1
	v_add_co_u32_e32 v228, vcc, s11, v86
	v_lshl_add_u64 v[178:179], v[170:171], 0, v[190:191]
	v_lshl_add_u64 v[180:181], v[170:171], 0, v[192:193]
	global_load_dwordx4 v[170:173], v[88:89], off sc1
	v_addc_co_u32_e32 v229, vcc, 0, v87, vcc
	s_waitcnt lgkmcnt(1)
	v_mfma_f32_32x32x16_f16 v[2:17], v[82:85], v[126:129], v[2:17]
	s_lshl_b32 s22, s21, 3
	v_sub_u32_e32 v74, s22, v199
	v_add_u32_e32 v74, v74, v203
	v_add_u32_e32 v75, 24, v74
	v_cmp_gt_i32_e32 vcc, 0, v74
	s_min_i32 s22, s12, s9
	s_ashr_i32 s23, s22, 31
	s_waitcnt lgkmcnt(0)
	v_mfma_f32_32x32x16_f16 v[50:65], v[82:85], v[166:169], v[50:65]
	global_load_dwordx4 v[94:97], v[174:175], off nt
	global_load_dwordx4 v[90:93], v[176:177], off nt
	global_load_dwordx4 v[86:89], v[178:179], off nt
	global_load_dwordx4 v[82:85], v[180:181], off nt
	v_add_u32_e32 v178, -16, v215
	v_cndmask_b32_e32 v74, v74, v75, vcc
	v_mul_lo_u32 v74, v74, s2
	v_cmp_gt_u32_e32 vcc, s3, v178
	v_add3_u32 v179, s24, v210, v208
	s_lshl_b64 s[22:23], s[22:23], 15
	v_mfma_f32_32x32x16_f16 v[34:49], v[162:165], v[126:129], v[34:49]
	global_load_dwordx4 v[126:129], v[226:227], off sc1
	global_load_dwordx4 v[174:177], v[228:229], off sc1
	ds_write_b128 v224, v[110:113]
	s_waitcnt vmcnt(16)
	ds_write_b128 v223, v[118:121] offset:24576
	s_waitcnt lgkmcnt(0)
	s_barrier
	v_cndmask_b32_e32 v74, v206, v74, vcc
	v_add_u32_e32 v178, v214, v74
	v_mfma_f32_32x32x16_f16 v[18:33], v[162:165], v[166:169], v[18:33]
	ds_read_b128 v[110:113], v219
	ds_read_b128 v[118:121], v230
	ds_read_b128 v[162:165], v230 offset:512
	ds_read_b128 v[166:169], v219 offset:512
	ds_write2st64_b64 v178, v[80:81], v[76:77] offset1:1
	s_waitcnt lgkmcnt(3)
	v_mfma_f32_32x32x16_f16 v[2:17], v[110:113], v[118:121], v[2:17]
	s_waitcnt lgkmcnt(2)
	v_mfma_f32_32x32x16_f16 v[50:65], v[110:113], v[162:165], v[50:65]
	s_waitcnt lgkmcnt(1)
	v_mfma_f32_32x32x16_f16 v[34:49], v[166:169], v[118:121], v[34:49]
	ds_read_b128 v[74:77], v220
	ds_read_b128 v[78:81], v179
	ds_read_b128 v[110:113], v179 offset:512
	ds_read_b128 v[118:121], v220 offset:512
	ds_write2st64_b64 v178, v[72:73], v[68:69] offset0:2 offset1:3
	v_mfma_f32_32x32x16_f16 v[18:33], v[166:169], v[162:165], v[18:33]
	v_add3_u32 v162, s24, v212, v208
	s_waitcnt lgkmcnt(3)
	v_mfma_f32_32x32x16_f16 v[2:17], v[74:77], v[78:81], v[2:17]
	s_waitcnt lgkmcnt(2)
	v_mfma_f32_32x32x16_f16 v[50:65], v[74:77], v[110:113], v[50:65]
	v_add3_u32 v74, s24, v211, v208
	s_mul_i32 s24, s13, 0x4080
	s_add_i32 s13, s18, 7
	s_min_i32 s13, s13, s14
	s_add_u32 s22, s6, s22
	s_addc_u32 s23, s7, s23
	v_add3_u32 v226, s24, v207, v208
	s_waitcnt lgkmcnt(1)
	v_mfma_f32_32x32x16_f16 v[34:49], v[118:121], v[78:81], v[34:49]
	ds_read_b128 v[66:69], v221
	ds_read_b128 v[70:73], v74
	ds_read_b128 v[74:77], v74 offset:512
	ds_read_b128 v[78:81], v221 offset:512
	s_waitcnt vmcnt(10)
	ds_write_b128 v184, v[106:109] offset:51600
	ds_write_b128 v184, v[114:117] offset:59792
	v_mfma_f32_32x32x16_f16 v[18:33], v[118:121], v[110:113], v[18:33]
	v_lshl_add_u32 v110, s13, 6, v213
	v_lshl_add_u64 v[118:119], s[22:23], 0, v[184:185]
	global_load_dwordx4 v[178:181], v[118:119], off sc1
	v_add_co_u32_e32 v168, vcc, s10, v118
	v_lshl_add_u64 v[120:121], s[22:23], 0, v[182:183]
	s_nop 0
	v_addc_co_u32_e32 v169, vcc, 0, v119, vcc
	s_waitcnt lgkmcnt(4)
	v_mfma_f32_32x32x16_f16 v[2:17], v[66:69], v[70:73], v[2:17]
	s_add_i32 s13, s21, 1
	s_cmp_lg_u32 s21, 2
	s_cselect_b32 s13, s13, 0
	s_lshl_b32 s22, s13, 3
	s_mul_i32 s23, s21, 0x4080
	s_add_i32 s21, s18, 8
	s_min_i32 s25, s21, s14
	s_waitcnt lgkmcnt(3)
	v_mfma_f32_32x32x16_f16 v[50:65], v[66:69], v[74:77], v[50:65]
	v_max_i32_e32 v66, 0, v110
	v_min_i32_e32 v66, s8, v66
	v_ashrrev_i32_e32 v67, 31, v66
	v_lshl_add_u64 v[166:167], v[66:67], 2, s[4:5]
	ds_read_b128 v[66:69], v222
	v_add3_u32 v232, s23, v210, v208
	s_waitcnt lgkmcnt(3)
	v_mfma_f32_32x32x16_f16 v[34:49], v[78:81], v[70:73], v[34:49]
	ds_read_b128 v[110:113], v222 offset:512
	ds_read_b128 v[70:73], v162
	ds_read_b128 v[114:117], v162 offset:512
	global_load_dwordx4 v[162:165], v[120:121], off sc1
	v_cvt_pk_f16_f32 v121, v156, v157
	v_cvt_pk_f16_f32 v120, v154, v155
	v_add3_u32 v154, s24, v210, v208
	v_mfma_f32_32x32x16_f16 v[18:33], v[78:81], v[74:77], v[18:33]
	v_add_co_u32_e32 v74, vcc, s11, v118
	v_lshl_add_u64 v[76:77], v[166:167], 0, v[186:187]
	s_nop 0
	v_addc_co_u32_e32 v75, vcc, 0, v119, vcc
	v_lshl_add_u64 v[118:119], v[166:167], 0, v[192:193]
	s_waitcnt lgkmcnt(1)
	v_mfma_f32_32x32x16_f16 v[2:17], v[66:69], v[70:73], v[2:17]
	s_waitcnt lgkmcnt(0)
	v_mfma_f32_32x32x16_f16 v[50:65], v[66:69], v[114:117], v[50:65]
	v_lshl_add_u64 v[66:67], v[166:167], 0, v[188:189]
	v_lshl_add_u64 v[68:69], v[166:167], 0, v[190:191]
	global_load_dwordx4 v[106:109], v[168:169], off sc1
	s_nop 0
	global_load_dwordx4 v[166:169], v[74:75], off sc1
	global_load_dwordx4 v[78:81], v[76:77], off nt
	s_nop 0
	global_load_dwordx4 v[74:77], v[66:67], off nt
	v_mfma_f32_32x32x16_f16 v[34:49], v[110:113], v[70:73], v[34:49]
	global_load_dwordx4 v[70:73], v[68:69], off nt
	s_nop 0
	global_load_dwordx4 v[66:69], v[118:119], off nt
	s_waitcnt vmcnt(17)
	ds_write_b128 v182, v[98:101] offset:51600
	s_waitcnt vmcnt(16)
	ds_write_b128 v200, v[102:105] offset:51600
	s_waitcnt lgkmcnt(0)
	s_barrier
	v_cvt_pk_f16_f32 v119, v160, v161
	v_cvt_pk_f16_f32 v118, v158, v159
	v_mfma_f32_32x32x16_f16 v[18:33], v[110:113], v[114:117], v[18:33]
	ds_read_b128 v[98:101], v225 offset:51600
	ds_read_b128 v[102:105], v226
	ds_read_b128 v[110:113], v226 offset:512
	ds_read_b128 v[114:117], v225 offset:52112
	v_add_u32_e32 v225, -8, v215
	s_waitcnt lgkmcnt(2)
	v_mfma_f32_32x32x16_f16 v[2:17], v[98:101], v[102:105], v[2:17]
	s_waitcnt lgkmcnt(1)
	v_mfma_f32_32x32x16_f16 v[50:65], v[98:101], v[110:113], v[50:65]
	v_sub_u32_e32 v98, s22, v199
	v_add_u32_e32 v98, v98, v203
	v_add_u32_e32 v99, 24, v98
	v_cmp_gt_i32_e32 vcc, 0, v98
	s_nop 1
	v_cndmask_b32_e32 v98, v98, v99, vcc
	v_mul_lo_u32 v98, v98, s2
	v_cmp_gt_u32_e32 vcc, s3, v225
	s_waitcnt lgkmcnt(0)
	v_mfma_f32_32x32x16_f16 v[34:49], v[114:117], v[102:105], v[34:49]
	v_add3_u32 v225, s23, v207, v208
	v_cndmask_b32_e32 v98, v206, v98, vcc
	v_add_u32_e32 v155, v214, v98
	ds_write2st64_b64 v155, v[118:119], v[120:121] offset1:1
	v_add3_u32 v118, s24, v211, v208
	v_mfma_f32_32x32x16_f16 v[18:33], v[114:117], v[110:113], v[18:33]
	ds_read_b128 v[98:101], v216 offset:51600
	ds_read_b128 v[102:105], v154
	ds_read_b128 v[110:113], v154 offset:512
	ds_read_b128 v[114:117], v216 offset:52112
	v_add3_u32 v154, s24, v212, v208
	s_add_i32 s24, s18, 5
	s_min_i32 s24, s24, s9
	s_waitcnt lgkmcnt(2)
	v_mfma_f32_32x32x16_f16 v[2:17], v[98:101], v[102:105], v[2:17]
	s_waitcnt lgkmcnt(1)
	v_mfma_f32_32x32x16_f16 v[50:65], v[98:101], v[110:113], v[50:65]
	v_cvt_pk_f16_f32 v99, v144, v145
	v_cvt_pk_f16_f32 v98, v142, v143
	v_cvt_pk_f16_f32 v101, v140, v141
	v_cvt_pk_f16_f32 v100, v138, v139
	ds_write2st64_b64 v155, v[98:99], v[100:101] offset0:2 offset1:3
	s_waitcnt lgkmcnt(1)
	v_mfma_f32_32x32x16_f16 v[34:49], v[114:117], v[102:105], v[34:49]
	v_mfma_f32_32x32x16_f16 v[18:33], v[114:117], v[110:113], v[18:33]
	ds_read_b128 v[98:101], v217 offset:51600
	ds_read_b128 v[102:105], v118
	ds_read_b128 v[110:113], v118 offset:512
	ds_read_b128 v[114:117], v217 offset:52112
	v_lshl_add_u32 v118, s25, 6, v213
	s_ashr_i32 s25, s24, 31
	s_lshl_b64 s[24:25], s[24:25], 15
	s_add_u32 s24, s6, s24
	s_addc_u32 s25, s7, s25
	v_lshl_add_u64 v[120:121], s[24:25], 0, v[184:185]
	s_waitcnt lgkmcnt(2)
	v_mfma_f32_32x32x16_f16 v[2:17], v[98:101], v[102:105], v[2:17]
	v_lshl_add_u64 v[138:139], s[24:25], 0, v[182:183]
	s_add_i32 s22, s22, 8
	s_cmp_lg_u32 s13, 2
	s_cselect_b32 s22, s22, 0
	s_waitcnt lgkmcnt(1)
	v_mfma_f32_32x32x16_f16 v[50:65], v[98:101], v[110:113], v[50:65]
	v_max_i32_e32 v98, 0, v118
	v_min_i32_e32 v98, s8, v98
	v_ashrrev_i32_e32 v99, 31, v98
	v_lshl_add_u64 v[118:119], v[98:99], 2, s[4:5]
	v_lshl_add_u64 v[140:141], v[118:119], 0, v[186:187]
	v_lshl_add_u64 v[142:143], v[118:119], 0, v[188:189]
	v_lshl_add_u64 v[144:145], v[118:119], 0, v[190:191]
	s_waitcnt lgkmcnt(0)
	v_mfma_f32_32x32x16_f16 v[34:49], v[114:117], v[102:105], v[34:49]
	ds_read_b128 v[98:101], v218 offset:51600
	ds_read_b128 v[102:105], v218 offset:52112
	s_waitcnt vmcnt(15)
	ds_write_b128 v223, v[122:125]
	s_waitcnt vmcnt(9)
	ds_write_b128 v223, v[126:129] offset:8192
	v_add_co_u32_e32 v122, vcc, s10, v120
	v_lshl_add_u64 v[118:119], v[118:119], 0, v[192:193]
	s_nop 0
	v_addc_co_u32_e32 v123, vcc, 0, v121, vcc
	v_mfma_f32_32x32x16_f16 v[18:33], v[114:117], v[110:113], v[18:33]
	ds_read_b128 v[114:117], v154
	ds_read_b128 v[226:229], v154 offset:512
	global_load_dwordx4 v[126:129], v[120:121], off sc1
	global_load_dwordx4 v[110:113], v[138:139], off sc1
	global_load_dwordx4 v[158:161], v[140:141], off nt
	global_load_dwordx4 v[154:157], v[142:143], off nt
	s_nop 0
	global_load_dwordx4 v[142:145], v[144:145], off nt
	s_nop 0
	global_load_dwordx4 v[138:141], v[118:119], off nt
	s_waitcnt lgkmcnt(1)
	v_mfma_f32_32x32x16_f16 v[2:17], v[98:101], v[114:117], v[2:17]
	s_waitcnt lgkmcnt(0)
	v_mfma_f32_32x32x16_f16 v[50:65], v[98:101], v[226:229], v[50:65]
	v_add_co_u32_e32 v98, vcc, s11, v120
	s_nop 1
	v_addc_co_u32_e32 v99, vcc, 0, v121, vcc
	global_load_dwordx4 v[122:125], v[122:123], off sc1
	s_nop 0
	global_load_dwordx4 v[118:121], v[98:99], off sc1
	ds_write_b128 v224, v[170:173]
	s_waitcnt vmcnt(16)
	ds_write_b128 v223, v[174:177] offset:24576
	v_mfma_f32_32x32x16_f16 v[34:49], v[102:105], v[114:117], v[34:49]
	s_waitcnt lgkmcnt(0)
	s_barrier
	v_mfma_f32_32x32x16_f16 v[18:33], v[102:105], v[226:229], v[18:33]
	ds_read_b128 v[98:101], v219
	ds_read_b128 v[102:105], v225
	ds_read_b128 v[114:117], v225 offset:512
	ds_read_b128 v[170:173], v219 offset:512
	s_waitcnt lgkmcnt(2)
	v_mfma_f32_32x32x16_f16 v[2:17], v[98:101], v[102:105], v[2:17]
	s_waitcnt lgkmcnt(1)
	v_mfma_f32_32x32x16_f16 v[50:65], v[98:101], v[114:117], v[50:65]
	s_waitcnt vmcnt(30)
	v_cvt_pk_f16_f32 v153, v152, v153
	v_cvt_pk_f16_f32 v152, v150, v151
	v_cvt_pk_f16_f32 v149, v148, v149
	v_cvt_pk_f16_f32 v148, v146, v147
	v_sub_u32_e32 v98, s22, v199
	v_add_u32_e32 v98, v98, v203
	v_add_u32_e32 v99, 24, v98
	v_cmp_gt_i32_e32 vcc, 0, v98
	s_add_i32 s22, s18, 9
	s_min_i32 s22, s22, s14
	v_cndmask_b32_e32 v98, v98, v99, vcc
	v_mul_lo_u32 v98, v98, s2
	v_cmp_gt_u32_e32 vcc, s3, v215
	s_waitcnt lgkmcnt(0)
	v_mfma_f32_32x32x16_f16 v[34:49], v[170:173], v[102:105], v[34:49]
	s_min_i32 s18, s19, s9
	v_cndmask_b32_e32 v98, v206, v98, vcc
	v_add_u32_e32 v150, v214, v98
	ds_write2st64_b64 v150, v[152:153], v[148:149] offset1:1
	s_ashr_i32 s19, s18, 31
	s_lshl_b64 s[18:19], s[18:19], 15
	s_add_u32 s18, s6, s18
	v_mfma_f32_32x32x16_f16 v[18:33], v[170:173], v[114:117], v[18:33]
	ds_read_b128 v[98:101], v220
	ds_read_b128 v[102:105], v232
	ds_read_b128 v[114:117], v232 offset:512
	ds_read_b128 v[146:149], v220 offset:512
	s_addc_u32 s19, s7, s19
	v_lshl_add_u64 v[224:225], s[18:19], 0, v[184:185]
	v_add_co_u32_e32 v228, vcc, s10, v224
	v_lshl_add_u64 v[226:227], s[18:19], 0, v[182:183]
	s_nop 0
	v_addc_co_u32_e32 v229, vcc, 0, v225, vcc
	s_waitcnt lgkmcnt(2)
	v_mfma_f32_32x32x16_f16 v[2:17], v[98:101], v[102:105], v[2:17]
	v_add_u32_e32 v215, 32, v215
	s_cmp_le_i32 s21, s14
	s_waitcnt lgkmcnt(1)
	v_mfma_f32_32x32x16_f16 v[50:65], v[98:101], v[114:117], v[50:65]
	v_cvt_pk_f16_f32 v99, v136, v137
	v_cvt_pk_f16_f32 v98, v134, v135
	v_cvt_pk_f16_f32 v101, v132, v133
	v_cvt_pk_f16_f32 v100, v130, v131
	v_add3_u32 v130, s23, v211, v208
	ds_write2st64_b64 v150, v[98:99], v[100:101] offset0:2 offset1:3
	v_lshl_add_u32 v134, s22, 6, v213
	s_waitcnt lgkmcnt(1)
	v_mfma_f32_32x32x16_f16 v[34:49], v[146:149], v[102:105], v[34:49]
	v_add3_u32 v136, s23, v212, v208
	v_mfma_f32_32x32x16_f16 v[18:33], v[146:149], v[114:117], v[18:33]
	ds_read_b128 v[98:101], v221
	ds_read_b128 v[102:105], v130
	ds_read_b128 v[114:117], v130 offset:512
	ds_read_b128 v[130:133], v221 offset:512
	s_waitcnt lgkmcnt(2)
	v_mfma_f32_32x32x16_f16 v[2:17], v[98:101], v[102:105], v[2:17]
	s_waitcnt lgkmcnt(1)
	v_mfma_f32_32x32x16_f16 v[50:65], v[98:101], v[114:117], v[50:65]
	v_max_i32_e32 v98, 0, v134
	v_min_i32_e32 v98, s8, v98
	v_ashrrev_i32_e32 v99, 31, v98
	v_lshl_add_u64 v[134:135], v[98:99], 2, s[4:5]
	ds_read_b128 v[98:101], v222
	ds_read_b128 v[170:173], v222 offset:512
	s_waitcnt vmcnt(15)
	ds_write_b128 v184, v[178:181] offset:51600
	s_waitcnt vmcnt(13)
	ds_write_b128 v184, v[106:109] offset:59792
	v_lshl_add_u64 v[106:107], v[134:135], 0, v[186:187]
	s_waitcnt lgkmcnt(4)
	v_mfma_f32_32x32x16_f16 v[34:49], v[130:133], v[102:105], v[34:49]
	ds_read_b128 v[102:105], v136
	ds_read_b128 v[174:177], v136 offset:512
	v_lshl_add_u64 v[108:109], v[134:135], 0, v[188:189]
	v_add_co_u32_e32 v178, vcc, s11, v224
	s_nop 1
	v_addc_co_u32_e32 v179, vcc, 0, v225, vcc
	v_mfma_f32_32x32x16_f16 v[18:33], v[130:133], v[114:117], v[18:33]
	v_lshl_add_u64 v[114:115], v[134:135], 0, v[190:191]
	v_lshl_add_u64 v[116:117], v[134:135], 0, v[192:193]
	s_waitcnt lgkmcnt(1)
	v_mfma_f32_32x32x16_f16 v[2:17], v[98:101], v[102:105], v[2:17]
	s_waitcnt lgkmcnt(0)
	v_mfma_f32_32x32x16_f16 v[50:65], v[98:101], v[174:177], v[50:65]
	global_load_dwordx4 v[150:153], v[106:107], off nt
	global_load_dwordx4 v[146:149], v[108:109], off nt
	global_load_dwordx4 v[134:137], v[114:115], off nt
	global_load_dwordx4 v[130:133], v[116:117], off nt
	s_nop 0
	global_load_dwordx4 v[106:109], v[224:225], off sc1
	global_load_dwordx4 v[114:117], v[228:229], off sc1
	global_load_dwordx4 v[98:101], v[226:227], off sc1
	v_mfma_f32_32x32x16_f16 v[34:49], v[170:173], v[102:105], v[34:49]
	global_load_dwordx4 v[102:105], v[178:179], off sc1
	ds_write_b128 v182, v[162:165] offset:51600
	s_waitcnt vmcnt(20)
	ds_write_b128 v200, v[166:169] offset:51600
	s_waitcnt lgkmcnt(0)
	s_barrier
	v_mfma_f32_32x32x16_f16 v[18:33], v[170:173], v[174:177], v[18:33]
	s_cbranch_scc1 .LBB6_106
	s_mov_b32 s18, s12
	s_branch .LBB6_109
